# PUp phase start: pair seltok loads (2 round trips instead of 4) and drop stale vmcnt(0) between first and remaining A staging loads
# baseline (speedup 1.0000x reference)
.LBB0_947:
	s_or_b64 exec, exec, s[30:31]
	v_mov_b32_e32 v6, v0
	s_mov_b64 s[0:1], 0
	v_readlane_b32 s36, v253, 8
	s_waitcnt lgkmcnt(0)
	s_barrier
	s_cmpk_lt_i32 s36, 0x1600
	v_readfirstlane_b32 s4, v6
	s_cbranch_scc0 .LBB0_972
	v_bfe_i32 v4, v6, 27, 1
	v_lshlrev_b32_e32 v2, 4, v6
	v_lshrrev_b32_e32 v4, 22, v4
	v_add_u32_e32 v4, v2, v4
	v_and_b32_e32 v4, 0xfffffc00, v4
	v_sub_u32_e32 v4, v2, v4
	v_readlane_b32 s8, v253, 40
	v_ashrrev_i32_e32 v3, 31, v6
	v_lshrrev_b32_e32 v5, 4, v4
	v_readlane_b32 s22, v253, 54
	v_lshrrev_b32_e32 v3, 26, v3
	v_bitop3_b32 v4, v5, v4, 32 bitop3:0x6c
	v_readlane_b32 s23, v253, 55
	s_add_u32 s5, s22, s0
	v_add_u32_e32 v3, v6, v3
	v_ashrrev_i32_e32 v7, 31, v4
	s_addc_u32 s1, s23, s1
	v_ashrrev_i32_e32 v3, 6, v3
	v_lshrrev_b32_e32 v7, 26, v7
	s_add_u32 s6, s5, 0x23000000
	v_lshlrev_b32_e32 v5, 3, v3
	v_add_u32_e32 v8, v4, v7
	s_addc_u32 s7, s1, 0
	v_and_b32_e32 v5, -16, v5
	v_ashrrev_i32_e32 v9, 6, v8
	s_add_u32 s0, s5, s97
	v_add_u32_e32 v7, v9, v5
	v_and_b32_e32 v5, 0xc0, v8
	s_addc_u32 s2, s1, 0
	v_sub_u32_e32 v4, v4, v5
	s_add_u32 s38, s0, 0xc00000
	v_lshlrev_b32_e32 v3, 5, v3
	v_ashrrev_i16_sdwa v4, v237, sext(v4) dst_sel:DWORD dst_unused:UNUSED_PAD src0_sel:DWORD src1_sel:BYTE_0
	v_lshlrev_b32_e32 v5, 1, v7
	v_lshrrev_b32_e32 v8, 2, v7
	v_and_b32_e32 v9, 3, v9
	s_mov_b32 s0, 0x3fffe0
	v_and_b32_e32 v3, 32, v3
	v_bfe_i32 v4, v4, 0, 16
	v_and_b32_e32 v5, 24, v5
	v_and_b32_e32 v8, 4, v8
	v_and_or_b32 v9, v7, s0, v9
	v_add_u32_e32 v2, 0x2000, v2
	v_or3_b32 v5, v9, v8, v5
	v_add_lshl_u32 v8, v3, v4, 1
	v_ashrrev_i32_e32 v3, 31, v2
	v_lshrrev_b32_e32 v3, 22, v3
	v_add_u32_e32 v3, v2, v3
	v_ashrrev_i32_e32 v3, 10, v3
	v_mul_i32_i24_e32 v4, 0x400, v3
	v_sub_u32_e32 v2, v2, v4
	v_lshrrev_b32_e32 v4, 4, v2
	v_bitop3_b32 v2, v4, v2, 32 bitop3:0x6c
	v_lshl_add_u32 v194, v5, 10, v8
	v_ashrrev_i32_e32 v5, 31, v2
	v_lshrrev_b32_e32 v5, 26, v5
	s_addc_u32 s39, s2, 0
	v_lshlrev_b32_e32 v4, 3, v3
	v_add_u32_e32 v5, v2, v5
	v_readlane_b32 s9, v253, 41
	s_add_u32 s8, s5, 0x170000
	v_and_b32_e32 v4, -16, v4
	v_ashrrev_i32_e32 v10, 6, v5
	s_addc_u32 s9, s1, 0
	v_add_u32_e32 v9, v10, v4
	v_and_b32_e32 v10, 3, v10
	s_ashr_i32 s40, s36, 31
	v_and_or_b32 v10, v9, s0, v10
	s_lshr_b32 s0, s40, 29
	v_readlane_b32 s17, v253, 49
	v_and_b32_e32 v4, 0xc0, v5
	s_add_i32 s0, s36, s0
	v_readlane_b32 s10, v253, 42
	v_readlane_b32 s16, v253, 48
	v_sub_u32_e32 v2, v2, v4
	s_ashr_i32 s17, s4, 6
	s_ashr_i32 s2, s0, 3
	s_and_b32 s0, s0, -8
	s_ashr_i32 s16, s4, 8
	v_lshlrev_b32_e32 v3, 5, v3
	v_ashrrev_i16_sdwa v2, v237, sext(v2) dst_sel:DWORD dst_unused:UNUSED_PAD src0_sel:DWORD src1_sel:BYTE_0
	v_lshlrev_b32_e32 v4, 1, v9
	v_lshrrev_b32_e32 v5, 2, v9
	s_lshl_b32 s10, s17, 10
	s_sub_i32 s0, s36, s0
	v_and_b32_e32 v3, 32, v3
	v_bfe_i32 v2, v2, 0, 16
	v_and_b32_e32 v4, 24, v4
	v_and_b32_e32 v5, 4, v5
	s_cmp_lt_i32 s0, 0
	s_movk_i32 s3, 0x2c1
	v_or3_b32 v4, v10, v5, v4
	v_add_lshl_u32 v10, v3, v2, 1
	s_cselect_b32 s3, s3, 0x2c0
	v_mov_b32_e32 v2, v0
	s_mul_i32 s0, s3, s0
	s_add_i32 s0, s0, s2
	v_ashrrev_i32_e32 v3, 31, v2
	v_lshrrev_b32_e32 v3, 26, v3
	s_mul_hi_i32 s2, s0, 0x2e8ba2e9
	v_lshlrev_b32_e32 v12, 4, v2
	v_add_u32_e32 v3, v2, v3
	v_bfe_i32 v2, v2, 27, 1
	s_lshr_b32 s3, s2, 31
	s_ashr_i32 s2, s2, 4
	v_lshrrev_b32_e32 v2, 22, v2
	s_add_i32 s2, s2, s3
	v_add_u32_e32 v2, v12, v2
	s_lshl_b32 s3, s2, 2
	s_mulk_i32 s2, 0x58
	v_and_b32_e32 v2, 0xfffffc00, v2
	s_sub_i32 s2, s0, s2
	v_sub_u32_e32 v2, v12, v2
	v_lshl_add_u32 v162, v4, 10, v10
	s_bfe_i32 s0, s2, 0x80000
	v_lshrrev_b32_e32 v4, 4, v2
	v_readlane_b32 s11, v253, 43
	s_bfe_u32 s0, s0, 0x2000d
	v_bitop3_b32 v2, v4, v2, 32 bitop3:0x6c
	s_add_i32 s11, s2, s0
	v_ashrrev_i32_e32 v5, 31, v2
	s_bfe_i32 s0, s11, 0x80000
	s_and_b32 s11, s11, 0xfc
	v_lshrrev_b32_e32 v5, 26, v5
	s_sub_i32 s2, s2, s11
	v_add_u32_e32 v5, v2, v5
	s_sext_i32_i8 s2, s2
	v_ashrrev_i32_e32 v3, 6, v3
	v_ashrrev_i32_e32 v11, 6, v5
	v_and_b32_e32 v5, 0xc0, v5
	v_readlane_b32 s13, v253, 45
	s_add_i32 s55, s3, s2
	v_lshlrev_b32_e32 v4, 3, v3
	v_sub_u32_e32 v2, v2, v5
	s_lshl_b32 s13, s55, 8
	v_and_b32_e32 v4, -16, v4
	v_lshlrev_b32_e32 v3, 5, v3
	v_ashrrev_i16_sdwa v2, v237, sext(v2) dst_sel:DWORD dst_unused:UNUSED_PAD src0_sel:DWORD src1_sel:BYTE_0
	v_and_b32_e32 v3, 32, v3
	v_bfe_i32 v5, v2, 0, 16
	v_add3_u32 v2, v4, s13, v11
	v_add_lshl_u32 v11, v3, v5, 1
	v_ashrrev_i32_e32 v3, 31, v2
	v_lshl_add_u64 v[4:5], v[2:3], 2, s[8:9]
	global_load_dword v3, v[4:5], off
	global_load_dword v13, v[4:5], off offset:512
	v_add_u32_e32 v2, 0x80, v2
	s_sext_i32_i16 s0, s0
	v_readlane_b32 s12, v253, 44
	s_lshr_b32 s0, s0, 2
	s_ashr_i32 s12, s55, 4
	s_bfe_i64 s[2:3], s[0:1], 0x100000
	s_mul_hi_i32 s11, s12, 0x580000
	s_mul_i32 s12, s12, 0x580000
	s_lshl_b64 s[2:3], s[2:3], 18
	s_add_u32 s12, s38, s12
	s_addc_u32 s11, s39, s11
	s_add_u32 s12, s12, s2
	v_mov_b32_e32 v163, v195
	v_readlane_b32 s14, v253, 46
	v_readlane_b32 s15, v253, 47
	v_readlane_b32 s18, v253, 50
	v_readlane_b32 s19, v253, 51
	v_readlane_b32 s20, v253, 52
	v_readlane_b32 s21, v253, 53
	s_waitcnt vmcnt(0)
	v_lshl_add_u32 v164, v3, 10, v11
	v_lshl_add_u32 v11, v13, 10, v11
	v_add_u32_e32 v2, 0x2000, v12
	v_ashrrev_i32_e32 v3, 31, v2
	v_lshrrev_b32_e32 v3, 22, v3
	v_add_u32_e32 v3, v2, v3
	v_ashrrev_i32_e32 v3, 10, v3
	v_mul_i32_i24_e32 v4, 0x400, v3
	v_sub_u32_e32 v2, v2, v4
	v_lshrrev_b32_e32 v4, 4, v2
	v_bitop3_b32 v2, v4, v2, 32 bitop3:0x6c
	v_ashrrev_i32_e32 v5, 31, v2
	v_lshrrev_b32_e32 v5, 26, v5
	v_add_u32_e32 v5, v2, v5
	v_ashrrev_i32_e32 v12, 6, v5
	v_and_b32_e32 v5, 0xc0, v5
	v_lshlrev_b32_e32 v4, 3, v3
	v_sub_u32_e32 v2, v2, v5
	v_and_b32_e32 v4, -16, v4
	v_lshlrev_b32_e32 v3, 5, v3
	v_ashrrev_i16_sdwa v2, v237, sext(v2) dst_sel:DWORD dst_unused:UNUSED_PAD src0_sel:DWORD src1_sel:BYTE_0
	v_and_b32_e32 v3, 32, v3
	v_bfe_i32 v5, v2, 0, 16
	v_add3_u32 v2, v4, s13, v12
	v_add_lshl_u32 v12, v3, v5, 1
	v_ashrrev_i32_e32 v3, 31, v2
	v_lshl_add_u64 v[4:5], v[2:3], 2, s[8:9]
	global_load_dword v3, v[4:5], off
	global_load_dword v14, v[4:5], off offset:512
	v_add_u32_e32 v2, 0x80, v2
	s_addc_u32 s13, s11, s3
	s_add_i32 s41, s10, 0
	s_add_i32 s42, s41, 0x10000
	s_add_i32 s43, s41, 0x12000
	s_mov_b32 m0, s42
	s_add_u32 s2, s12, 0x20000
	s_addc_u32 s3, s13, 0
	s_add_i32 s44, s41, 0x14000
	s_add_i32 s45, s41, 0x16000
	s_add_i32 s46, s41, 0x2000
	s_add_i32 s47, s41, 0x4000
	s_add_i32 s48, s41, 0x6000
	s_cmp_eq_u32 s16, 1
	v_lshl_add_u64 v[4:5], s[12:13], 0, v[162:163]
	s_cselect_b64 s[10:11], -1, 0
	s_cmp_lg_u32 s16, 1
	s_waitcnt vmcnt(0)
	v_lshl_add_u32 v166, v3, 10, v12
	s_waitcnt vmcnt(0)
	global_load_lds_dwordx4 v194, s[12:13]
	s_mov_b32 m0, s43
	v_lshl_add_u32 v168, v14, 10, v12
	global_load_lds_dwordx4 v162, s[12:13]
	s_mov_b32 m0, s44
	v_lshl_add_u64 v[2:3], s[12:13], 0, v[194:195]
	global_load_lds_dwordx4 v194, s[2:3]
	s_mov_b32 m0, s45
	s_nop 0
	global_load_lds_dwordx4 v162, s[2:3]
	s_mov_b32 m0, s41
	s_nop 0
	global_load_lds_dwordx4 v164, s[6:7]
	s_mov_b32 m0, s46
	s_nop 0
	global_load_lds_dwordx4 v166, s[6:7]
	s_mov_b32 m0, s47
	s_nop 0
	global_load_lds_dwordx4 v11, s[6:7]
	s_mov_b32 m0, s48
	s_nop 0
	global_load_lds_dwordx4 v168, s[6:7]
	s_cbranch_scc1 .LBB0_950
	s_barrier
